# attn_kv_tile_loads_batched
# baseline (speedup 1.0000x reference)
.LBB0_388:
	s_bfe_u32 s12, s19, 0x70001
	s_lshl_b32 s13, s12, 7
	s_and_b32 s9, s19, 1
	s_add_i32 s14, s13, 0xffffff80
	s_ashr_i32 s8, s19, 8
	s_lshl_b32 s62, s9, 7
	s_lshl_b32 s15, s8, 14
	v_lshl_add_u64 v[8:9], v[66:67], 0, s[62:63]
	v_add_u32_e32 v3, s14, v80
	v_cmp_gt_u32_e32 vcc, s70, v3
	v_mov_b32_e32 v12, 0
	v_mov_b32_e32 v13, 0
	v_mov_b32_e32 v14, 0
	v_mov_b32_e32 v15, 0
	s_and_saveexec_b64 s[10:11], vcc
	s_cbranch_execz .Lattn_ld_k0
	v_or_b32_e32 v4, s15, v3
	v_ashrrev_i32_e32 v5, 31, v4
	v_lshlrev_b64 v[4:5], 8, v[4:5]
	v_lshl_add_u64 v[4:5], v[8:9], 0, v[4:5]
	global_load_dwordx4 v[12:15], v[4:5], off
.Lattn_ld_k0:
	s_or_b64 exec, exec, s[10:11]
	v_add_u32_e32 v3, s14, v81
	v_cmp_gt_u32_e32 vcc, s70, v3
	v_mov_b32_e32 v16, 0
	v_mov_b32_e32 v17, 0
	v_mov_b32_e32 v18, 0
	v_mov_b32_e32 v19, 0
	s_and_saveexec_b64 s[10:11], vcc
	s_cbranch_execz .Lattn_ld_k1
	v_or_b32_e32 v4, s15, v3
	v_ashrrev_i32_e32 v5, 31, v4
	v_lshlrev_b64 v[4:5], 8, v[4:5]
	v_lshl_add_u64 v[4:5], v[8:9], 0, v[4:5]
	global_load_dwordx4 v[16:19], v[4:5], off
.Lattn_ld_k1:
	s_or_b64 exec, exec, s[10:11]
	v_add_u32_e32 v3, s14, v82
	v_cmp_gt_u32_e32 vcc, s70, v3
	v_mov_b32_e32 v20, 0
	v_mov_b32_e32 v21, 0
	v_mov_b32_e32 v22, 0
	v_mov_b32_e32 v23, 0
	s_and_saveexec_b64 s[10:11], vcc
	s_cbranch_execz .Lattn_ld_k2
	v_or_b32_e32 v4, s15, v3
	v_ashrrev_i32_e32 v5, 31, v4
	v_lshlrev_b64 v[4:5], 8, v[4:5]
	v_lshl_add_u64 v[4:5], v[8:9], 0, v[4:5]
	global_load_dwordx4 v[20:23], v[4:5], off
.Lattn_ld_k2:
	s_or_b64 exec, exec, s[10:11]
	v_add_u32_e32 v3, s14, v83
	v_cmp_gt_u32_e32 vcc, s70, v3
	v_mov_b32_e32 v24, 0
	v_mov_b32_e32 v25, 0
	v_mov_b32_e32 v26, 0
	v_mov_b32_e32 v27, 0
	s_and_saveexec_b64 s[10:11], vcc
	s_cbranch_execz .Lattn_ld_k3
	v_or_b32_e32 v4, s15, v3
	v_ashrrev_i32_e32 v5, 31, v4
	v_lshlrev_b64 v[4:5], 8, v[4:5]
	v_lshl_add_u64 v[4:5], v[8:9], 0, v[4:5]
	global_load_dwordx4 v[24:27], v[4:5], off
.Lattn_ld_k3:
	s_or_b64 exec, exec, s[10:11]
	v_add_u32_e32 v3, s14, v84
	v_cmp_gt_u32_e32 vcc, s70, v3
	v_mov_b32_e32 v28, 0
	v_mov_b32_e32 v29, 0
	v_mov_b32_e32 v30, 0
	v_mov_b32_e32 v31, 0
	s_and_saveexec_b64 s[10:11], vcc
	s_cbranch_execz .Lattn_ld_k4
	v_or_b32_e32 v4, s15, v3
	v_ashrrev_i32_e32 v5, 31, v4
	v_lshlrev_b64 v[4:5], 8, v[4:5]
	v_lshl_add_u64 v[4:5], v[8:9], 0, v[4:5]
	global_load_dwordx4 v[28:31], v[4:5], off
.Lattn_ld_k4:
	s_or_b64 exec, exec, s[10:11]
	v_add_u32_e32 v3, s14, v85
	v_cmp_gt_u32_e32 vcc, s70, v3
	v_mov_b32_e32 v32, 0
	v_mov_b32_e32 v33, 0
	v_mov_b32_e32 v34, 0
	v_mov_b32_e32 v35, 0
	s_and_saveexec_b64 s[10:11], vcc
	s_cbranch_execz .Lattn_ld_k5
	v_or_b32_e32 v4, s15, v3
	v_ashrrev_i32_e32 v5, 31, v4
	v_lshlrev_b64 v[4:5], 8, v[4:5]
	v_lshl_add_u64 v[4:5], v[8:9], 0, v[4:5]
	global_load_dwordx4 v[32:35], v[4:5], off
.Lattn_ld_k5:
	s_or_b64 exec, exec, s[10:11]
	s_lshl_b32 s10, s9, 6
	s_lshl_b32 s11, s8, 7
	s_or_b32 s15, s11, s10
	v_add_u32_e32 v194, s14, v87
	v_cmp_gt_u32_e32 vcc, s70, v194
	v_mov_b32_e32 v36, 0
	v_mov_b32_e32 v37, 0
	v_mov_b32_e32 v38, 0
	v_mov_b32_e32 v39, 0
	s_and_saveexec_b64 s[10:11], vcc
	s_cbranch_execz .Lattn_ld_v0
	v_add_u32_e32 v4, s15, v86
	v_ashrrev_i32_e32 v5, 31, v4
	v_lshlrev_b64 v[4:5], 15, v[4:5]
	v_lshl_add_u64 v[4:5], s[6:7], 0, v[4:5]
	v_lshl_add_u64 v[4:5], v[194:195], 1, v[4:5]
	global_load_dwordx4 v[36:39], v[4:5], off
.Lattn_ld_v0:
	s_or_b64 exec, exec, s[10:11]
	v_add_u32_e32 v194, s14, v89
	v_cmp_gt_u32_e32 vcc, s70, v194
	v_mov_b32_e32 v40, 0
	v_mov_b32_e32 v41, 0
	v_mov_b32_e32 v42, 0
	v_mov_b32_e32 v43, 0
	s_and_saveexec_b64 s[10:11], vcc
	s_cbranch_execz .Lattn_ld_v1
	v_add_u32_e32 v4, s15, v88
	v_ashrrev_i32_e32 v5, 31, v4
	v_lshlrev_b64 v[4:5], 15, v[4:5]
	v_lshl_add_u64 v[4:5], s[6:7], 0, v[4:5]
	v_lshl_add_u64 v[4:5], v[194:195], 1, v[4:5]
	global_load_dwordx4 v[40:43], v[4:5], off
.Lattn_ld_v1:
	s_or_b64 exec, exec, s[10:11]
	v_add_u32_e32 v194, s14, v91
	v_cmp_gt_u32_e32 vcc, s70, v194
	v_mov_b32_e32 v44, 0
	v_mov_b32_e32 v45, 0
	v_mov_b32_e32 v46, 0
	v_mov_b32_e32 v47, 0
	s_and_saveexec_b64 s[10:11], vcc
	s_cbranch_execz .Lattn_ld_v2
	v_add_u32_e32 v4, s15, v90
	v_ashrrev_i32_e32 v5, 31, v4
	v_lshlrev_b64 v[4:5], 15, v[4:5]
	v_lshl_add_u64 v[4:5], s[6:7], 0, v[4:5]
	v_lshl_add_u64 v[4:5], v[194:195], 1, v[4:5]
	global_load_dwordx4 v[44:47], v[4:5], off
.Lattn_ld_v2:
	s_or_b64 exec, exec, s[10:11]
	v_add_u32_e32 v194, s14, v93
	v_cmp_gt_u32_e32 vcc, s70, v194
	v_mov_b32_e32 v48, 0
	v_mov_b32_e32 v49, 0
	v_mov_b32_e32 v50, 0
	v_mov_b32_e32 v51, 0
	s_and_saveexec_b64 s[10:11], vcc
	s_cbranch_execz .Lattn_ld_v3
	v_add_u32_e32 v4, s15, v92
	v_ashrrev_i32_e32 v5, 31, v4
	v_lshlrev_b64 v[4:5], 15, v[4:5]
	v_lshl_add_u64 v[4:5], s[6:7], 0, v[4:5]
	v_lshl_add_u64 v[4:5], v[194:195], 1, v[4:5]
	global_load_dwordx4 v[48:51], v[4:5], off
.Lattn_ld_v3:
	s_or_b64 exec, exec, s[10:11]
	v_add_u32_e32 v194, s14, v95
	v_cmp_gt_u32_e32 vcc, s70, v194
	v_mov_b32_e32 v52, 0
	v_mov_b32_e32 v53, 0
	v_mov_b32_e32 v54, 0
	v_mov_b32_e32 v55, 0
	s_and_saveexec_b64 s[10:11], vcc
	s_cbranch_execz .Lattn_ld_v4
	v_add_u32_e32 v4, s15, v94
	v_ashrrev_i32_e32 v5, 31, v4
	v_lshlrev_b64 v[4:5], 15, v[4:5]
	v_lshl_add_u64 v[4:5], s[6:7], 0, v[4:5]
	v_lshl_add_u64 v[4:5], v[194:195], 1, v[4:5]
	global_load_dwordx4 v[52:55], v[4:5], off
.Lattn_ld_v4:
	s_or_b64 exec, exec, s[10:11]
	v_add_u32_e32 v194, s14, v97
	v_cmp_gt_u32_e32 vcc, s70, v194
	v_mov_b32_e32 v56, 0
	v_mov_b32_e32 v57, 0
	v_mov_b32_e32 v58, 0
	v_mov_b32_e32 v59, 0
	s_and_saveexec_b64 s[10:11], vcc
	s_cbranch_execz .Lattn_ld_v5
	v_add_u32_e32 v4, s15, v96
	v_ashrrev_i32_e32 v5, 31, v4
	v_lshlrev_b64 v[4:5], 15, v[4:5]
	v_lshl_add_u64 v[4:5], s[6:7], 0, v[4:5]
	v_lshl_add_u64 v[4:5], v[194:195], 1, v[4:5]
	global_load_dwordx4 v[56:59], v[4:5], off
.Lattn_ld_v5:
	s_or_b64 exec, exec, s[10:11]
	s_waitcnt lgkmcnt(0)
	s_barrier
	s_waitcnt vmcnt(0)
	ds_write_b128 v105, v[12:15]
	ds_write_b128 v106, v[16:19]
	ds_write_b128 v107, v[20:23]
	ds_write_b128 v108, v[24:27]
	ds_write_b128 v109, v[28:31]
	ds_write_b128 v110, v[32:35]
	ds_write2_b64 v111, v[36:37], v[38:39] offset1:1
	ds_write2_b64 v112, v[40:41], v[42:43] offset1:1
	ds_write2_b64 v113, v[44:45], v[46:47] offset1:1
	ds_write2_b64 v114, v[48:49], v[50:51] offset1:1
	ds_write2_b64 v115, v[52:53], v[54:55] offset1:1
	ds_write2_b64 v116, v[56:57], v[58:59] offset1:1
	s_and_saveexec_b64 s[10:11], s[2:3]
	s_xor_b64 s[10:11], exec, s[10:11]
	ds_write2st64_b32 v78, v236, v236 offset1:8
	s_or_saveexec_b64 s[10:11], s[10:11]
	s_lshl_b32 s9, s9, 2
	v_mov_b32_e32 v2, 0xf149f2ca
	v_mov_b32_e32 v3, 0xf149f2ca
	s_xor_b64 exec, exec, s[10:11]
	s_cbranch_execz .LBB0_416
	v_readlane_b32 s40, v253, 10
	v_or_b32_e32 v194, s9, v98
	v_readlane_b32 s42, v253, 12
	v_readlane_b32 s43, v253, 13
	v_readlane_b32 s41, v253, 11
	v_readlane_b32 s44, v253, 14
	v_lshl_add_u64 v[2:3], v[194:195], 2, s[42:43]
	global_load_dwordx4 v[2:5], v[2:3], off
	v_readlane_b32 s45, v253, 15
	v_readlane_b32 s46, v253, 16
	v_readlane_b32 s47, v253, 17
	v_readlane_b32 s48, v253, 18
	v_readlane_b32 s49, v253, 19
	v_readlane_b32 s50, v253, 20
	v_readlane_b32 s51, v253, 21
	v_readlane_b32 s52, v253, 22
	v_readlane_b32 s53, v253, 23
	v_readlane_b32 s54, v253, 24
	v_readlane_b32 s55, v253, 25
	s_waitcnt vmcnt(0)
	v_mul_f32_e32 v2, 0x3fb8aa3b, v2
	v_mul_f32_e32 v3, 0x3fb8aa3b, v3
	ds_write2st64_b32 v78, v2, v3 offset1:8
	v_pk_mul_f32 v[2:3], v[4:5], s[96:97] op_sel_hi:[1,0]
